# baseline (speedup 1.0000x reference)
.Lbc_scan:
	v_lshlrev_b32_e32 v1, 3, v0
	ds_read_b64 v[8:9], v1
	s_waitcnt lgkmcnt(0)
	v_add_u32_e32 v10, v8, v9
	v_mov_b32_e32 v11, v10
	s_nop 1
	v_add_u32_dpp v11, v11, v11 row_shr:1 row_mask:0xf bank_mask:0xf bound_ctrl:0
	s_nop 1
	v_add_u32_dpp v11, v11, v11 row_shr:2 row_mask:0xf bank_mask:0xf bound_ctrl:0
	s_nop 1
	v_add_u32_dpp v11, v11, v11 row_shr:4 row_mask:0xf bank_mask:0xf bound_ctrl:0
	s_nop 1
	v_add_u32_dpp v11, v11, v11 row_shr:8 row_mask:0xf bank_mask:0xf bound_ctrl:0
	s_nop 1
	v_add_u32_dpp v11, v11, v11 row_bcast:15 row_mask:0xa bank_mask:0xf
	s_nop 1
	v_add_u32_dpp v11, v11, v11 row_bcast:31 row_mask:0xc bank_mask:0xf
	v_lshrrev_b32_e32 v12, 6, v0
	s_nop 0
	v_readfirstlane_b32 s3, v12
	v_readlane_b32 s16, v11, 63
	s_lshl_b32 s17, s3, 2
	s_add_u32 s17, s17, 0x1020
	v_mov_b32_e32 v12, s16
	v_mov_b32_e32 v13, s17
	s_mov_b64 s[32:33], exec
	s_mov_b64 exec, 1
	ds_write_b32 v13, v12
	s_mov_b64 exec, s[32:33]
	s_waitcnt lgkmcnt(0)
	s_barrier
	v_mov_b32_e32 v13, 0x1020
	ds_read_b128 v[12:15], v13
	v_mov_b32_e32 v2, 0
	s_waitcnt lgkmcnt(0)
	s_cmp_gt_u32 s3, 0
	s_cselect_b32 s16, 1, 0
	v_mad_u32_u24 v2, v12, s16, v2
	s_cmp_gt_u32 s3, 1
	s_cselect_b32 s16, 1, 0
	v_mad_u32_u24 v2, v13, s16, v2
	s_cmp_gt_u32 s3, 2
	s_cselect_b32 s16, 1, 0
	v_mad_u32_u24 v2, v14, s16, v2
	v_sub_u32_e32 v4, v11, v10
	v_add_u32_e32 v4, v4, v2
	v_add_u32_e32 v5, v4, v8
	ds_write_b64 v1, v[4:5] offset:2048
	v_add_u32_e32 v6, s14, v4
	v_add_u32_e32 v7, s14, v5
	v_lshlrev_b32_e32 v12, 1, v0
	v_add_lshl_u32 v13, v12, s20, 2
	v_cmp_gt_u32_e32 vcc, s22, v12
	s_and_saveexec_b64 s[32:33], vcc
	s_cbranch_execz .Lbc_nooff
	global_store_dwordx2 v13, v[6:7], s[8:9] sc1
